# speedup vs baseline: 1.1549x; 1.0306x over previous
.LBB5_15:
	s_or_b64 exec, exec, s[6:7]
	s_load_dwordx4 s[4:7], s[0:1], 0x18
	v_mov_b32_e32 v17, 0
	s_waitcnt lgkmcnt(0)
	s_barrier
	ds_read_b32 v17, v17 offset:32776
	s_and_b32 s17, s5, 0xffff
	s_and_b32 s21, s15, 0xffff
	v_accvgpr_read_b32 v56, a0
	v_lshlrev_b32_e32 v15, 12, v1
	v_lshlrev_b32_e32 v18, 4, v56
	s_add_u32 s8, s4, s7
	s_mov_b32 s16, s4
	v_lshlrev_b32_e32 v14, 14, v10
	v_lshlrev_b32_e32 v16, 7, v0
	s_addc_u32 s9, s5, 0
	s_waitcnt lgkmcnt(0)
	v_cmp_ne_u32_e64 s[4:5], 0, v17
	v_add_u32_e32 v17, 0, v15
	v_or_b32_e32 v15, v18, v15
	v_or3_b32 v15, v16, v14, v15
	v_lshlrev_b32_e32 v13, 3, v0
	v_accvgpr_write_b32 a98, v15
	v_and_b32_e32 v15, 63, v57
	v_lshlrev_b32_e32 v19, 4, v13
	v_lshrrev_b32_e32 v15, 5, v15
	s_waitcnt vmcnt(1)
	v_mul_f32_e32 v45, 0xbfb8aa3b, v6
	v_mul_f32_e32 v6, 0xbfb8aa3b, v7
	v_mul_f32_e32 v7, 0xbfb8aa3b, v9
	v_lshlrev_b32_e32 v9, 8, v1
	v_add3_u32 v17, v17, v19, v18
	v_accvgpr_write_b32 a94, v15
	v_bfe_u32 v16, v57, 2, 3
	v_lshlrev_b32_e32 v15, 3, v57
	v_add_u32_e32 v9, v23, v9
	v_accvgpr_write_b32 a97, v17
	v_and_b32_e32 v17, 24, v15
	v_lshlrev_b32_e32 v10, 13, v10
	v_lshlrev_b32_e32 v15, 10, v16
	v_or_b32_e32 v9, v9, v13
	v_or3_b32 v10, v10, v15, v17
	v_cmp_eq_u32_e64 s[2:3], 3, v1
	v_lshl_add_u32 v9, v9, 1, s6
	v_accvgpr_write_b32 a95, v16
	v_lshl_add_u32 v16, v10, 1, s44
	v_lshlrev_b32_e32 v1, 7, v1
	v_and_b32_e32 v10, 8, v57
	v_lshlrev_b32_e32 v0, 1, v0
	v_or3_b32 v1, v1, v10, v0
	v_add_u32_e32 v10, s24, v9
	s_lshl_b32 s6, s33, 9
	v_or3_b32 v1, v1, v18, v14
	v_accvgpr_write_b32 a99, v10
	v_add_u32_e32 v10, s26, v9
	v_add_u32_e32 v1, s6, v1
	s_and_b32 s33, s6, 0xe00
	s_lshl_b32 s6, s42, 9
	v_accvgpr_write_b32 a102, v10
	v_add_u32_e32 v10, s28, v9
	s_and_b32 s35, s6, 0xe00
	s_lshl_b32 s6, s43, 9
	v_accvgpr_write_b32 a103, v10
	v_add_u32_e32 v10, s30, v9
	s_and_b32 s37, s6, 0xe00
	s_lshl_b32 s6, s45, 9
	v_accvgpr_write_b32 a104, v10
	v_add_u32_e32 v10, s34, v9
	v_accvgpr_write_b32 a96, v17
	v_ashrrev_i32_e32 v17, 31, v16
	s_and_b32 s39, s6, 0xe00
	s_lshl_b32 s6, s46, 9
	v_accvgpr_write_b32 a105, v10
	v_add_u32_e32 v10, s36, v9
	v_accvgpr_write_b32 a93, v17
	s_and_b32 s41, s6, 0xe00
	s_lshl_b32 s6, s47, 9
	v_accvgpr_write_b32 a106, v10
	v_add_u32_e32 v10, s38, v9
	v_add_u32_e32 v9, s40, v9
	v_or_b32_e32 v13, v13, v56
	v_accvgpr_write_b32 a92, v16
	v_lshl_add_u64 v[16:17], s[8:9], 0, v[16:17]
	s_and_b32 s42, s6, 0xe00
	s_lshl_b32 s6, s48, 9
	v_accvgpr_write_b32 a108, v9
	v_lshlrev_b32_e32 v9, 1, v12
	s_mov_b32 s19, 0x20000
	v_accvgpr_write_b32 a101, v17
	s_and_b32 s43, s6, 0xe00
	s_lshl_b32 s6, s49, 9
	v_accvgpr_write_b32 a107, v10
	v_add3_u32 v0, 0, v9, v0
	v_lshlrev_b32_e32 v9, 9, v11
	v_lshlrev_b32_e32 v10, 4, v13
	s_brev_b32 s18, -2
	s_mov_b32 s22, 0x80000
	s_mov_b32 s23, s19
	s_mov_b32 s20, s14
	v_cmp_gt_u32_e64 s[0:1], 8, v22
	s_mov_b32 s15, 0
	v_accvgpr_write_b32 a100, v16
	s_and_b32 s44, s6, 0xe00
	v_add3_u32 v9, 0, v9, v10
	s_mov_b64 s[26:27], 0
	s_mov_b32 s34, 0x80008000
	s_mov_b32 s36, 0x100000
	s_brev_b32 s38, 60
	s_mov_b32 s40, 0xbc38aa3b
	s_mov_b32 s45, 0x41000000
	s_waitcnt vmcnt(0)
	v_accvgpr_write_b32 a112, v250
	v_accvgpr_write_b32 a113, v251
	v_accvgpr_write_b32 a114, v252
	v_accvgpr_write_b32 a115, v253
	v_accvgpr_write_b32 a116, v2
	v_accvgpr_write_b32 a117, v3
	v_accvgpr_write_b32 a118, v4
	v_accvgpr_write_b32 a119, v5
	v_and_b32_e32 v46, 1, v57
	v_cmp_ne_u32_e64 s[0:1], 0, v46
	v_and_b32_e32 v46, 32, v57
	v_cmp_ne_u32_e64 s[30:31], 0, v46
	v_mov_b32_e32 v26, 0x44444444
	v_mov_b32_e32 v46, 0xeeeeeeee
	v_cndmask_b32_e64 v26, v26, v46, s[0:1]
	v_accvgpr_read_b32 v46, a98
	v_bfe_u32 v47, v57, 4, 2
	v_lshlrev_b32_e32 v47, 7, v47
	v_sub_u32_e32 v46, v46, v47
	v_and_b32_e32 v47, 7, v57
	v_lshlrev_b32_e32 v47, 4, v47
	v_sub_u32_e32 v46, v46, v47
	v_bfe_u32 v47, v57, 4, 1
	v_lshl_add_u32 v46, v47, 8, v46
	v_and_b32_e32 v47, 15, v57
	v_lshl_add_u32 v46, v47, 4, v46
	v_mov_b32_e32 v47, s33
	v_mov_b32_e32 v48, s35
	v_cndmask_b32_e64 v47, v47, v48, s[30:31]
	v_or_b32_e32 v27, v46, v47
	v_mov_b32_e32 v47, s37
	v_mov_b32_e32 v48, s39
	v_cndmask_b32_e64 v47, v47, v48, s[30:31]
	v_or_b32_e32 v28, v46, v47
	v_mov_b32_e32 v47, s41
	v_mov_b32_e32 v48, s42
	v_cndmask_b32_e64 v47, v47, v48, s[30:31]
	v_or_b32_e32 v29, v46, v47
	v_mov_b32_e32 v47, s43
	v_mov_b32_e32 v48, s44
	v_cndmask_b32_e64 v47, v47, v48, s[30:31]
	v_or_b32_e32 v30, v46, v47
	v_lshrrev_b32_e32 v46, 6, v57
	v_lshlrev_b32_e32 v46, 7, v46
	v_and_b32_e32 v47, 8, v57
	v_bfe_u32 v48, v57, 4, 2
	v_lshl_or_b32 v47, v48, 1, v47
	v_add_u32_e32 v46, v46, v47
	v_and_b32_e32 v47, 7, v57
	v_lshl_add_u32 v46, v47, 4, v46
	v_sub_u32_e32 v1, v1, v46
	v_bfe_u32 v46, v57, 7, 1
	v_lshlrev_b32_e32 v46, 8, v46
	v_and_b32_e32 v47, 7, v57
	v_lshl_or_b32 v46, v47, 5, v46
	v_bfe_u32 v47, v57, 5, 1
	v_lshl_or_b32 v46, v47, 4, v46
	v_bfe_u32 v47, v57, 3, 1
	v_bfe_u32 v48, v57, 6, 1
	v_lshl_or_b32 v47, v48, 1, v47
	v_lshl_or_b32 v46, v47, 2, v46
	v_bfe_u32 v47, v57, 4, 1
	v_lshl_or_b32 v46, v47, 1, v46
	v_add_u32_e32 v1, v1, v46
	v_lshrrev_b32_e32 v46, 6, v57
	v_lshlrev_b32_e32 v46, 12, v46
	v_bfe_u32 v47, v57, 4, 2
	v_lshl_or_b32 v46, v47, 10, v46
	v_and_b32_e32 v47, 3, v57
	v_lshl_or_b32 v46, v47, 2, v46
	v_bfe_u32 v47, v57, 3, 1
	v_bfe_u32 v48, v57, 4, 1
	v_xor_b32_e32 v47, v47, v48
	v_lshl_or_b32 v46, v47, 5, v46
	v_bfe_u32 v47, v57, 5, 1
	v_lshl_or_b32 v46, v47, 7, v46
	v_bfe_u32 v47, v57, 2, 1
	v_lshl_or_b32 v31, v47, 4, v46
	v_xor_b32_e32 v32, 0x80, v31
	v_xor_b32_e32 v47, 1, v47
	v_lshl_or_b32 v33, v47, 4, v46
	v_add_u32_e32 v33, 0x200, v33
	v_xor_b32_e32 v34, 0x80, v33
	v_lshrrev_b32_e32 v46, 3, v57
	v_and_b32_e32 v46, 24, v46
	v_lshrrev_b32_e32 v47, 1, v57
	v_and_or_b32 v46, v47, 4, v46
	v_bfe_u32 v47, v57, 4, 2
	v_or_b32_e32 v46, v46, v47
	v_and_b32_e32 v47, 3, v57
	v_and_b32_e32 v48, 4, v57
	v_lshl_or_b32 v47, v48, 1, v47
	v_xor_b32_e32 v46, v46, v47
	v_and_b32_e32 v47, 7, v57
	v_lshlrev_b32_e32 v47, 9, v47
	v_lshl_or_b32 v9, v46, 4, v47
	v_accvgpr_write_b32 a120, v226
	v_accvgpr_write_b32 a121, v227
	v_accvgpr_write_b32 a122, v228
	v_accvgpr_write_b32 a123, v229
	v_accvgpr_write_b32 a124, v230
	v_accvgpr_write_b32 a125, v231
	v_accvgpr_write_b32 a126, v232
	v_accvgpr_write_b32 a127, v233
	v_accvgpr_write_b32 a128, v234
	v_accvgpr_write_b32 a129, v235
	v_accvgpr_write_b32 a130, v236
	v_accvgpr_write_b32 a131, v237
	v_accvgpr_write_b32 a132, v238
	v_accvgpr_write_b32 a133, v239
	v_accvgpr_write_b32 a134, v240
	v_accvgpr_write_b32 a135, v241
	v_accvgpr_write_b32 a136, v242
	v_accvgpr_write_b32 a137, v243
	v_accvgpr_write_b32 a138, v244
	v_accvgpr_write_b32 a139, v245
	v_accvgpr_write_b32 a140, v246
	v_accvgpr_write_b32 a141, v247
	v_accvgpr_write_b32 a142, v248
	v_accvgpr_write_b32 a143, v249
	v_accvgpr_write_b32 a144, v194
	v_accvgpr_write_b32 a145, v195
	v_accvgpr_write_b32 a146, v196
	v_accvgpr_write_b32 a147, v197
	v_accvgpr_write_b32 a148, v198
	v_accvgpr_write_b32 a149, v199
	v_accvgpr_write_b32 a150, v200
	v_accvgpr_write_b32 a151, v201
	v_accvgpr_write_b32 a152, v202
	v_accvgpr_write_b32 a153, v203
	v_accvgpr_write_b32 a154, v204
	v_accvgpr_write_b32 a155, v205
	v_accvgpr_write_b32 a156, v206
	v_accvgpr_write_b32 a157, v207
	v_accvgpr_write_b32 a158, v208
	v_accvgpr_write_b32 a159, v209
	v_accvgpr_write_b32 a160, v210
	v_accvgpr_write_b32 a161, v211
	v_accvgpr_write_b32 a162, v212
	v_accvgpr_write_b32 a163, v213
	v_accvgpr_write_b32 a164, v214
	v_accvgpr_write_b32 a165, v215
	v_accvgpr_write_b32 a166, v216
	v_accvgpr_write_b32 a167, v217
	v_accvgpr_write_b32 a168, v218
	v_accvgpr_write_b32 a169, v219
	v_accvgpr_write_b32 a170, v220
	v_accvgpr_write_b32 a171, v221
	v_accvgpr_write_b32 a172, v222
	v_accvgpr_write_b32 a173, v223
	v_accvgpr_write_b32 a174, v224
	v_accvgpr_write_b32 a175, v225
	s_mov_b64 s[24:25], 0
	s_mov_b32 s46, 0
	s_mov_b32 s30, 0x3c38aa3b
	s_mov_b32 s31, 0xbc000000
	v_bfe_u32 v50, v57, 4, 2
	v_lshlrev_b32_e32 v50, 4, v50
	v_bfe_u32 v51, v57, 4, 1
	v_and_b32_e32 v52, 1, v57
	v_lshlrev_b32_e32 v52, 2, v52
	v_lshl_or_b32 v51, v51, 5, v52
	v_sub_u32_e32 v54, v51, v50
	v_bfe_u32 v51, v57, 1, 3
	v_and_b32_e32 v52, 7, v57
	v_sub_u32_e32 v51, v51, v52
	v_lshlrev_b32_e32 v51, 11, v51
	v_add_u32_e32 v54, v54, v51
	v_and_b32_e32 v55, 32, v57
	v_cmp_ne_u32_e64 s[28:29], 0, v55
	v_accvgpr_read_b32 v242, a99
	v_accvgpr_read_b32 v55, a102
	v_cndmask_b32_e64 v242, v242, v55, s[28:29]
	v_add_u32_e32 v242, v242, v54
	v_accvgpr_read_b32 v243, a103
	v_accvgpr_read_b32 v55, a104
	v_cndmask_b32_e64 v243, v243, v55, s[28:29]
	v_add_u32_e32 v243, v243, v54
	v_accvgpr_read_b32 v244, a105
	v_accvgpr_read_b32 v55, a106
	v_cndmask_b32_e64 v244, v244, v55, s[28:29]
	v_add_u32_e32 v244, v244, v54
	v_accvgpr_read_b32 v245, a107
	v_accvgpr_read_b32 v55, a108
	v_cndmask_b32_e64 v245, v245, v55, s[28:29]
	v_add_u32_e32 v245, v245, v54
	s_mov_b64 s[26:27], -1
	v_mov_b32_e32 v10, 0
	v_mov_b32_e32 v11, 0
	v_mov_b32_e32 v12, 0
	v_mov_b32_e32 v13, 0
	v_mov_b32_e32 v14, 0
	v_mov_b32_e32 v15, 0
	v_mov_b32_e32 v16, 0
	v_mov_b32_e32 v17, 0
	v_mov_b32_e32 v18, 0
	v_mov_b32_e32 v19, 0
	v_mov_b32_e32 v20, 0
	v_mov_b32_e32 v21, 0
	v_mov_b32_e32 v22, 0
	v_mov_b32_e32 v23, 0
	v_mov_b32_e32 v24, 0
	v_mov_b32_e32 v25, 0
	v_mov_b32_e32 v2, 0
	v_mov_b32_e32 v3, 0
	v_mov_b32_e32 v4, 0
	v_mov_b32_e32 v5, 0
	v_mov_b32_e32 v250, 0
	v_mov_b32_e32 v251, 0
	v_mov_b32_e32 v252, 0
	v_mov_b32_e32 v253, 0
	v_mov_b32_e32 v46, 0
	v_mov_b32_e32 v47, 0
	v_mov_b32_e32 v48, 0
	v_mov_b32_e32 v49, 0
	v_mov_b32_e32 v50, 0
	v_mov_b32_e32 v51, 0
	v_mov_b32_e32 v52, 0
	v_mov_b32_e32 v53, 0
	buffer_load_dword v226, v242, s[16:19], 0 offen sc1
	buffer_load_dword v227, v242, s[16:19], 0 offen offset:8 sc1
	buffer_load_dword v228, v242, s[16:19], 0 offen offset:16 sc1
	buffer_load_dword v229, v242, s[16:19], 0 offen offset:24 sc1
	buffer_load_dword v230, v243, s[16:19], 0 offen sc1
	buffer_load_dword v231, v243, s[16:19], 0 offen offset:8 sc1
	buffer_load_dword v232, v243, s[16:19], 0 offen offset:16 sc1
	buffer_load_dword v233, v243, s[16:19], 0 offen offset:24 sc1
	buffer_load_dword v234, v244, s[16:19], 0 offen sc1
	buffer_load_dword v235, v244, s[16:19], 0 offen offset:8 sc1
	buffer_load_dword v236, v244, s[16:19], 0 offen offset:16 sc1
	buffer_load_dword v237, v244, s[16:19], 0 offen offset:24 sc1
	buffer_load_dword v238, v245, s[16:19], 0 offen sc1
	buffer_load_dword v239, v245, s[16:19], 0 offen offset:8 sc1
	buffer_load_dword v240, v245, s[16:19], 0 offen offset:16 sc1
	buffer_load_dword v241, v245, s[16:19], 0 offen offset:24 sc1
	s_waitcnt vmcnt(0)

.Lrec_tail:
	s_add_i32 s14, s46, 1
	s_lshl_b32 s6, s14, 13
	s_lshl_b32 s7, s14, 17
	s_and_b32 s6, s6, 0x8000
	s_and_b32 s7, s7, 0x60000
	v_add_f32_e32 v10, v10, v11
	v_add_f32_e32 v12, v12, v13
	v_add_f32_e32 v14, v14, v15
	v_add_f32_e32 v16, v16, v17
	ds_write2_b32 v31, v10, v14 offset0:0 offset1:16
	ds_write2_b32 v33, v12, v16 offset0:0 offset1:16
	v_add_f32_e32 v18, v18, v19
	v_add_f32_e32 v20, v20, v21
	v_add_f32_e32 v22, v22, v23
	v_add_f32_e32 v24, v24, v25
	ds_write2_b32 v32, v18, v22 offset0:0 offset1:16
	ds_write2_b32 v34, v20, v24 offset0:0 offset1:16
	v_add_f32_e32 v46, v46, v47
	v_add_f32_e32 v48, v48, v49
	v_add_f32_e32 v50, v50, v51
	v_add_f32_e32 v52, v52, v53
	ds_write2_b32 v31, v46, v50 offset0:64 offset1:80
	ds_write2_b32 v33, v48, v52 offset0:64 offset1:80
	v_add_f32_e32 v2, v2, v3
	v_add_f32_e32 v4, v4, v5
	v_add_f32_e32 v250, v250, v251
	v_add_f32_e32 v252, v252, v253
	ds_write2_b32 v32, v2, v250 offset0:64 offset1:80
	ds_write2_b32 v34, v4, v252 offset0:64 offset1:80
	s_waitcnt lgkmcnt(0)
	s_barrier
	ds_read_b128 v[10:13], v9
	ds_read_b128 v[14:17], v9 offset:4096
	ds_read_b128 v[18:21], v9 offset:8192
	ds_read_b128 v[22:25], v9 offset:12288
	s_min_u32 s29, s46, 0xfd
	s_lshl_b32 s29, s29, 19
	s_add_u32 s29, s29, s36
	v_mov_b32_e32 v54, s29
	v_add_co_u32_e32 v54, vcc, v254, v54
	s_nop 1
	v_addc_co_u32_e32 v55, vcc, 0, v255, vcc
	global_load_dwordx2 v[40:41], v[54:55], off
	s_waitcnt lgkmcnt(2)
	v_pk_add_f32 v[10:11], v[10:11], v[14:15]
	v_pk_add_f32 v[12:13], v[12:13], v[16:17]
	s_waitcnt lgkmcnt(0)
	v_pk_add_f32 v[18:19], v[18:19], v[22:23]
	v_pk_add_f32 v[20:21], v[20:21], v[24:25]
	v_pk_add_f32 v[10:11], v[10:11], v[18:19]
	v_pk_add_f32 v[12:13], v[12:13], v[20:21]
	v_fmac_f32_e32 v247, s48, v11
	v_fmac_f32_e32 v246, s48, v10
	v_fmac_f32_e32 v249, s48, v13
	v_fmac_f32_e32 v248, s47, v12
	v_exp_f32_e32 v15, v247
	v_exp_f32_e32 v14, v246
	v_exp_f32_e32 v17, v249
	v_max_f32_e32 v16, 0, v248
	v_add_f32_e32 v15, 1.0, v15
	v_add_f32_e32 v14, 1.0, v14
	v_add_f32_e32 v17, 1.0, v17
	v_rcp_f32_e32 v14, v14
	v_rcp_f32_e32 v15, v15
	v_rcp_f32_e32 v17, v17
	v_add_u32_e32 v18, s7, v1
	v_mul_f32_e32 v12, v16, v14
	v_fmac_f32_e32 v12, v44, v15
	v_max_f32_e32 v19, 0, v12
	v_mul_f32_e32 v13, v17, v19
	v_fma_mixlo_f16 v14, v13, s45, 0
	s_lshl_b32 s29, s46, 3
	v_and_b32_e32 v14, 0x7fff, v14
	s_andn2_b64 vcc, exec, s[4:5]
	v_or_b32_e32 v16, s6, v14
	s_cbranch_vccnz .Lrec_slowst
	buffer_store_short v16, v18, s[20:23], 0 offen
	s_branch .Lrec_stored

.Lrec_stored:
	s_cmpk_eq_i32 s14, 0x100
	s_cbranch_scc1 .Lrec_exit
	v_and_or_b32 v15, s29, 56, v56
	v_lshl_add_u32 v15, v15, 6, v0
	ds_write_b16 v15, v14 offset:33024
	v_mov_b32_e32 v44, v12
	v_add_u32_e32 v242, s7, v27
	v_add_u32_e32 v243, s7, v28
	v_add_u32_e32 v244, s7, v29
	v_add_u32_e32 v245, s7, v30
	v_xor_b32_e32 v31, 0x4000, v31
	v_xor_b32_e32 v32, 0x4000, v32
	v_xor_b32_e32 v33, 0x4000, v33
	v_xor_b32_e32 v34, 0x4000, v34
	v_xor_b32_e32 v9, 0x4000, v9
	v_mov_b32_e32 v10, 0
	v_mov_b32_e32 v11, 0
	v_mov_b32_e32 v12, 0
	v_mov_b32_e32 v13, 0
	v_mov_b32_e32 v14, 0
	v_mov_b32_e32 v15, 0
	v_mov_b32_e32 v16, 0
	v_mov_b32_e32 v17, 0
	v_mov_b32_e32 v18, 0
	v_mov_b32_e32 v19, 0
	v_mov_b32_e32 v20, 0
	v_mov_b32_e32 v21, 0
	v_mov_b32_e32 v22, 0
	v_mov_b32_e32 v23, 0
	v_mov_b32_e32 v24, 0
	v_mov_b32_e32 v25, 0
	v_mov_b32_e32 v2, 0
	v_mov_b32_e32 v3, 0
	v_mov_b32_e32 v4, 0
	v_mov_b32_e32 v5, 0
	v_mov_b32_e32 v250, 0
	v_mov_b32_e32 v251, 0
	v_mov_b32_e32 v252, 0
	v_mov_b32_e32 v253, 0
	buffer_load_dwordx4 v[226:229], v242, s[20:23], 0 offen sc1
	buffer_load_dwordx4 v[230:233], v243, s[20:23], 0 offen sc1
	buffer_load_dwordx4 v[234:237], v244, s[20:23], 0 offen sc1
	buffer_load_dwordx4 v[238:241], v245, s[20:23], 0 offen sc1
	s_mov_b64 s[26:27], s[24:25]
	s_cmp_eq_u64 s[2:3], 0
	s_cbranch_scc1 .Lrec_noflush
	s_and_b32 s29, s46, 3
	s_cmp_lg_u32 s29, 0
	s_cbranch_scc1 .Lrec_noflush
	s_cmp_lt_u32 s46, 4
	s_cbranch_scc1 .Lrec_noflush
	s_add_i32 s29, s46, -4
	v_accvgpr_read_b32 v46, a94
	v_or_b32_e32 v50, s29, v46
	v_lshlrev_b32_e32 v46, 3, v50
	v_accvgpr_read_b32 v47, a95
	v_and_or_b32 v46, v46, 40, v47
	v_accvgpr_read_b32 v47, a96
	v_lshl_add_u32 v47, v47, 1, 0
	v_lshl_add_u32 v54, v46, 6, v47
	ds_read_b128 v[46:49], v54 offset:33024
	v_ashrrev_i32_e32 v51, 31, v50
	v_accvgpr_read_b32 v52, a100
	v_lshlrev_b64 v[50:51], 17, v[50:51]
	v_accvgpr_read_b32 v53, a101
	v_lshl_add_u64 v[50:51], v[52:53], 0, v[50:51]
	v_add_co_u32_e32 v52, vcc, 0x20000, v50
	s_nop 1
	v_addc_co_u32_e32 v53, vcc, 0, v51, vcc
	s_waitcnt lgkmcnt(0)
	global_store_dwordx4 v[52:53], v[46:49], off
	s_nop 1
	ds_read_b128 v[46:49], v54 offset:34048
	v_add_co_u32_e32 v50, vcc, 0x60000, v50
	s_nop 1
	v_addc_co_u32_e32 v51, vcc, 0, v51, vcc
	s_waitcnt lgkmcnt(0)
	global_store_dwordx4 v[50:51], v[46:49], off
	s_nop 1
